# v9: v4b + spatial-gating unit: LDS reads of each k-step issued together ahead of the MFMAs
# speedup vs baseline: 1.0024x; 1.0024x over previous
; __device__ __forceinline__ unsigned f2bf(float f) { unsigned u = __builtin_bit_cast(unsigned, f); return (u + 0x7fffu + ((u >> 16) & 1u)) >> 16; }
; __device__ __forceinline__ void sg_phase(const Frame& F, const KArgs& a, const int u_first, const int u_count) {
;     ...
;         { const int s = s_; const f32x2 ms = st[s];
; #pragma unroll
;             for (int q = 0; q < 4; ++q) { const u32x4 raw = zraw[q]; const unsigned rw[4] = {raw.x, raw.y, raw.z, raw.w};
;                 const f32x4 g0 = lg[q][0], g1 = lg[q][1], b0 = lb[q][0], b1 = lb[q][1];
; #pragma unroll
;                 for (int i = 0; i < 8; ++i) { const unsigned wd = rw[i >> 1]; const float v = __builtin_bit_cast(float, (i & 1) ? (wd & 0xffff0000u) : (wd << 16));
;                     const float gg = (i < 4) ? g0[i & 3] : g1[i & 3], bb = (i < 4) ? b0[i & 3] : b1[i & 3];
;                     vt[(c0 + 8 * q + i) * 136 + (s ^ ((tid & 3) * 16))] = (unsigned short)f2bf((v - ms[0]) * ms[1] * gg + bb); } } }
.LBB0_814:
	s_or_b64 exec, exec, s[76:77]
	s_waitcnt lgkmcnt(0)
	s_barrier
	ds_read_b64 v[184:185], v179
	s_waitcnt vmcnt(27)
	v_lshlrev_b32_e32 v155, 16, v130
	v_and_b32_e32 v130, 0xffff0000, v130
	s_waitcnt vmcnt(10)
	v_cndmask_b32_e64 v62, v62, 0, s[12:13]
	v_cndmask_b32_e64 v63, v63, 0, s[14:15]
	s_waitcnt lgkmcnt(0)
	v_sub_f32_e32 v155, v155, v184
	v_mul_f32_e32 v155, v185, v155
	v_fma_f32 v138, v138, v155, v142
	v_sub_f32_e32 v130, v130, v184
	v_bfe_u32 v142, v138, 16, 1
	v_mul_f32_e32 v130, v185, v130
	v_add3_u32 v138, v138, v142, s91
	v_fma_f32 v130, v139, v130, v143
	ds_write_b16_d16_hi v183, v138 offset:1024
	v_bfe_u32 v138, v130, 16, 1
	v_add3_u32 v130, v130, v138, s91
	ds_write_b16_d16_hi v183, v130 offset:1296
	v_lshlrev_b32_e32 v130, 16, v131
	v_sub_f32_e32 v130, v130, v184
	v_mul_f32_e32 v130, v185, v130
	v_fma_f32 v130, v140, v130, v144
	v_bfe_u32 v138, v130, 16, 1
	v_add3_u32 v130, v130, v138, s91
	ds_write_b16_d16_hi v183, v130 offset:1568
	v_and_b32_e32 v130, 0xffff0000, v131
	v_sub_f32_e32 v130, v130, v184
	v_mul_f32_e32 v130, v185, v130
	v_fmac_f32_e32 v145, v141, v130
	v_bfe_u32 v130, v145, 16, 1
	v_add3_u32 v130, v145, v130, s91
	ds_write_b16_d16_hi v183, v130 offset:1840
	v_lshlrev_b32_e32 v130, 16, v132
	v_sub_f32_e32 v130, v130, v184
	v_mul_f32_e32 v130, v185, v130
	v_fma_f32 v126, v126, v130, v134
	v_bfe_u32 v130, v126, 16, 1
	v_add3_u32 v126, v126, v130, s91
	ds_write_b16_d16_hi v183, v126 offset:2112
	v_and_b32_e32 v126, 0xffff0000, v132
	v_sub_f32_e32 v126, v126, v184
	v_mul_f32_e32 v126, v185, v126
	v_fma_f32 v126, v127, v126, v135
	v_bfe_u32 v127, v126, 16, 1
	v_add3_u32 v126, v126, v127, s91
	ds_write_b16_d16_hi v183, v126 offset:2384
	v_lshlrev_b32_e32 v126, 16, v133
	v_sub_f32_e32 v126, v126, v184
	v_mul_f32_e32 v126, v185, v126
	v_fma_f32 v126, v128, v126, v136
	v_bfe_u32 v127, v126, 16, 1
	v_add3_u32 v126, v126, v127, s91
	ds_write_b16_d16_hi v183, v126 offset:2656
	v_and_b32_e32 v126, 0xffff0000, v133
	v_sub_f32_e32 v126, v126, v184
	v_mul_f32_e32 v126, v185, v126
	v_fmac_f32_e32 v137, v129, v126
	v_bfe_u32 v126, v137, 16, 1
	v_add3_u32 v126, v137, v126, s91
	ds_write_b16_d16_hi v183, v126 offset:2928
	v_lshlrev_b32_e32 v126, 16, v110
	v_sub_f32_e32 v126, v126, v184
	v_mul_f32_e32 v126, v185, v126
	v_and_b32_e32 v110, 0xffff0000, v110
	v_fma_f32 v118, v118, v126, v122
	v_sub_f32_e32 v110, v110, v184
	v_bfe_u32 v122, v118, 16, 1
	v_mul_f32_e32 v110, v185, v110
	v_add3_u32 v118, v118, v122, s91
	v_fma_f32 v110, v119, v110, v123
	ds_write_b16_d16_hi v183, v118 offset:3200
	v_bfe_u32 v118, v110, 16, 1
	v_add3_u32 v110, v110, v118, s91
	ds_write_b16_d16_hi v183, v110 offset:3472
	v_lshlrev_b32_e32 v110, 16, v111
	v_sub_f32_e32 v110, v110, v184
	v_mul_f32_e32 v110, v185, v110
	v_fma_f32 v110, v120, v110, v124
	v_bfe_u32 v118, v110, 16, 1
	v_add3_u32 v110, v110, v118, s91
	ds_write_b16_d16_hi v183, v110 offset:3744
	v_and_b32_e32 v110, 0xffff0000, v111
	v_sub_f32_e32 v110, v110, v184
	v_mul_f32_e32 v110, v185, v110
	v_fmac_f32_e32 v125, v121, v110
	v_bfe_u32 v110, v125, 16, 1
	v_add3_u32 v110, v125, v110, s91
	ds_write_b16_d16_hi v183, v110 offset:4016
	v_lshlrev_b32_e32 v110, 16, v112
	v_sub_f32_e32 v110, v110, v184
	v_mul_f32_e32 v110, v185, v110
	v_fma_f32 v106, v106, v110, v114
	v_bfe_u32 v110, v106, 16, 1
	v_add3_u32 v106, v106, v110, s91
	ds_write_b16_d16_hi v183, v106 offset:4288
	v_and_b32_e32 v106, 0xffff0000, v112
	v_sub_f32_e32 v106, v106, v184
	v_mul_f32_e32 v106, v185, v106
	v_fma_f32 v106, v107, v106, v115
	v_bfe_u32 v107, v106, 16, 1
	v_add3_u32 v106, v106, v107, s91
	ds_write_b16_d16_hi v183, v106 offset:4560
	v_lshlrev_b32_e32 v106, 16, v113
	v_sub_f32_e32 v106, v106, v184
	v_mul_f32_e32 v106, v185, v106
	v_fma_f32 v106, v108, v106, v116
	v_bfe_u32 v107, v106, 16, 1
	v_add3_u32 v106, v106, v107, s91
	ds_write_b16_d16_hi v183, v106 offset:4832
	v_and_b32_e32 v106, 0xffff0000, v113
	v_sub_f32_e32 v106, v106, v184
	v_mul_f32_e32 v106, v185, v106
	v_fmac_f32_e32 v117, v109, v106
	v_bfe_u32 v106, v117, 16, 1
	v_add3_u32 v106, v117, v106, s91
	ds_write_b16_d16_hi v183, v106 offset:5104
	v_lshlrev_b32_e32 v106, 16, v86
	v_sub_f32_e32 v106, v106, v184
	v_mul_f32_e32 v106, v185, v106
	v_and_b32_e32 v86, 0xffff0000, v86
	v_fma_f32 v98, v98, v106, v102
	v_sub_f32_e32 v86, v86, v184
	v_bfe_u32 v102, v98, 16, 1
	v_mul_f32_e32 v86, v185, v86
	v_add3_u32 v98, v98, v102, s91
	v_fma_f32 v86, v99, v86, v103
	ds_write_b16_d16_hi v183, v98 offset:5376
	v_bfe_u32 v98, v86, 16, 1
	v_add3_u32 v86, v86, v98, s91
	ds_write_b16_d16_hi v183, v86 offset:5648
	v_lshlrev_b32_e32 v86, 16, v87
	v_sub_f32_e32 v86, v86, v184
	v_mul_f32_e32 v86, v185, v86
	v_fma_f32 v86, v100, v86, v104
	v_bfe_u32 v98, v86, 16, 1
	v_add3_u32 v86, v86, v98, s91
	ds_write_b16_d16_hi v183, v86 offset:5920
	v_and_b32_e32 v86, 0xffff0000, v87
	v_sub_f32_e32 v86, v86, v184
	v_mul_f32_e32 v86, v185, v86
	v_fmac_f32_e32 v105, v101, v86
	v_bfe_u32 v86, v105, 16, 1
	v_add3_u32 v86, v105, v86, s91
	ds_write_b16_d16_hi v183, v86 offset:6192
	v_lshlrev_b32_e32 v86, 16, v88
	v_sub_f32_e32 v86, v86, v184
	v_mul_f32_e32 v86, v185, v86
	v_fma_f32 v86, v90, v86, v94
	v_bfe_u32 v87, v86, 16, 1
	v_add3_u32 v86, v86, v87, s91
	ds_write_b16_d16_hi v183, v86 offset:6464
	v_and_b32_e32 v86, 0xffff0000, v88
	v_sub_f32_e32 v86, v86, v184
	v_mul_f32_e32 v86, v185, v86
	v_fma_f32 v86, v91, v86, v95
	v_bfe_u32 v87, v86, 16, 1
	v_add3_u32 v86, v86, v87, s91
	ds_write_b16_d16_hi v183, v86 offset:6736
	v_lshlrev_b32_e32 v86, 16, v89
	v_sub_f32_e32 v86, v86, v184
	v_mul_f32_e32 v86, v185, v86
	v_fma_f32 v86, v92, v86, v96
	v_bfe_u32 v87, v86, 16, 1
	v_add3_u32 v86, v86, v87, s91
; __device__ __forceinline__ unsigned f2bf(float f) { unsigned u = __builtin_bit_cast(unsigned, f); return (u + 0x7fffu + ((u >> 16) & 1u)) >> 16; }
; #define LAS __attribute__((address_space(3)))
; __device__ __forceinline__ unsigned cvt_pk_bf16(float lo, float hi) { unsigned r; asm volatile("v_cvt_pk_bf16_f32 %0, %1, %2" : "=v"(r) : "v"(lo), "v"(hi)); return r; }
; __device__ __forceinline__ void sg_phase(const Frame& F, const KArgs& a, const int u_first, const int u_count) {
;     ...
;         { const int s = s_; const f32x2 ms = st[s];
; #pragma unroll
;             for (int q = 0; q < 4; ++q) { const u32x4 raw = zraw[q]; const unsigned rw[4] = {raw.x, raw.y, raw.z, raw.w};
;                 const f32x4 g0 = lg[q][0], g1 = lg[q][1], b0 = lb[q][0], b1 = lb[q][1];
; #pragma unroll
;                 for (int i = 0; i < 8; ++i) { const unsigned wd = rw[i >> 1]; const float v = __builtin_bit_cast(float, (i & 1) ? (wd & 0xffff0000u) : (wd << 16));
;                     const float gg = (i < 4) ? g0[i & 3] : g1[i & 3], bb = (i < 4) ? b0[i & 3] : b1[i & 3];
;                     vt[(c0 + 8 * q + i) * 136 + (s ^ ((tid & 3) * 16))] = (unsigned short)f2bf((v - ms[0]) * ms[1] * gg + bb); } } }
;         __syncthreads();
;         f32x4 acc[8];
; #pragma unroll
;         for (int j = 0; j < 8; ++j) acc[j] = (f32x4){0.f, 0.f, 0.f, 0.f};
; #pragma unroll
;         for (int ks = 0; ks < 4; ++ks) { if (ks > (w >> 1)) continue;
;             const f32x4 w0 = wraw[ks][0], w1 = wraw[ks][1];
;             float wv[8] = {w0[0], w0[1], w0[2], w0[3], w1[0], w1[1], w1[2], w1[3]};
; #pragma unroll
;             for (int i = 0; i < 8; ++i) if (32 * ks + 8 * kq + i > t) wv[i] = 0.f;
;             u32x4 pk; pk.x = cvt_pk_bf16(wv[0], wv[1]); pk.y = cvt_pk_bf16(wv[2], wv[3]); pk.z = cvt_pk_bf16(wv[4], wv[5]); pk.w = cvt_pk_bf16(wv[6], wv[7]);
;             const bf16x8 wf = __builtin_bit_cast(bf16x8, pk);
; #pragma unroll
;             for (int j = 0; j < 8; ++j) { const bf16x8 vf = *(const LAS bf16x8*)(vt + (16 * j + tl) * 136 + ((32 * ks + 8 * kq) ^ ((j >> 1) * 16)));
;                 acc[j] = __builtin_amdgcn_mfma_f32_16x16x32_bf16(vf, wf, acc[j], 0, 0, 0); }
;         }
	ds_write_b16_d16_hi v183, v86 offset:7008
	v_and_b32_e32 v86, 0xffff0000, v89
	v_sub_f32_e32 v86, v86, v184
	v_mul_f32_e32 v86, v185, v86
	v_fmac_f32_e32 v97, v93, v86
	v_bfe_u32 v86, v97, 16, 1
	v_add3_u32 v86, v97, v86, s91
	ds_write_b16_d16_hi v183, v86 offset:7280
	v_lshlrev_b32_e32 v86, 16, v58
	v_sub_f32_e32 v86, v86, v184
	v_mul_f32_e32 v86, v185, v86
	v_and_b32_e32 v58, 0xffff0000, v58
	v_fma_f32 v78, v78, v86, v82
	v_sub_f32_e32 v58, v58, v184
	v_bfe_u32 v82, v78, 16, 1
	v_mul_f32_e32 v58, v185, v58
	v_add3_u32 v78, v78, v82, s91
	v_fma_f32 v58, v79, v58, v83
	ds_write_b16_d16_hi v183, v78 offset:7552
	v_bfe_u32 v78, v58, 16, 1
	v_add3_u32 v58, v58, v78, s91
	ds_write_b16_d16_hi v183, v58 offset:7824
	v_lshlrev_b32_e32 v58, 16, v59
	v_sub_f32_e32 v58, v58, v184
	v_mul_f32_e32 v58, v185, v58
	v_fma_f32 v58, v80, v58, v84
	v_bfe_u32 v78, v58, 16, 1
	v_add3_u32 v58, v58, v78, s91
	ds_write_b16_d16_hi v183, v58 offset:8096
	v_and_b32_e32 v58, 0xffff0000, v59
	v_sub_f32_e32 v58, v58, v184
	v_mul_f32_e32 v58, v185, v58
	v_fmac_f32_e32 v85, v81, v58
	v_bfe_u32 v58, v85, 16, 1
	v_add3_u32 v58, v85, v58, s91
	ds_write_b16_d16_hi v183, v58 offset:8368
	v_lshlrev_b32_e32 v58, 16, v60
	v_sub_f32_e32 v58, v58, v184
	v_mul_f32_e32 v58, v185, v58
	v_fma_f32 v58, v66, v58, v70
	v_bfe_u32 v59, v58, 16, 1
	v_add3_u32 v58, v58, v59, s91
	ds_write_b16_d16_hi v183, v58 offset:8640
	v_and_b32_e32 v58, 0xffff0000, v60
	v_sub_f32_e32 v58, v58, v184
	v_mul_f32_e32 v58, v185, v58
	v_fma_f32 v58, v67, v58, v71
	v_bfe_u32 v59, v58, 16, 1
	v_add3_u32 v58, v58, v59, s91
	ds_write_b16_d16_hi v183, v58 offset:8912
	v_lshlrev_b32_e32 v58, 16, v61
	v_sub_f32_e32 v58, v58, v184
	v_mul_f32_e32 v58, v185, v58
	v_fma_f32 v58, v68, v58, v72
	v_bfe_u32 v59, v58, 16, 1
	v_add3_u32 v58, v58, v59, s91
	ds_write_b16_d16_hi v183, v58 offset:9184
	v_and_b32_e32 v58, 0xffff0000, v61
	v_sub_f32_e32 v58, v58, v184
	v_mul_f32_e32 v58, v185, v58
	v_fmac_f32_e32 v73, v69, v58
	v_bfe_u32 v58, v73, 16, 1
	v_add3_u32 v58, v73, v58, s91
	ds_write_b16_d16_hi v183, v58 offset:9456
	s_waitcnt vmcnt(9)
	v_cndmask_b32_e64 v58, v74, 0, s[4:5]
	v_cndmask_b32_e64 v59, 0, v75, s[6:7]
	v_cndmask_b32_e64 v58, v58, v74, s[6:7]
	v_cndmask_b32_e64 v60, v76, 0, s[8:9]
	v_cndmask_b32_e64 v61, v77, 0, s[10:11]
	v_cndmask_b32_e64 v64, v64, 0, s[16:17]
	v_cndmask_b32_e64 v65, v65, 0, s[18:19]
	s_waitcnt lgkmcnt(0)
	s_barrier
	v_cvt_pk_bf16_f32 v58, v58, v59
	v_cvt_pk_bf16_f32 v59, v60, v61
	v_cvt_pk_bf16_f32 v60, v62, v63
	v_cvt_pk_bf16_f32 v61, v64, v65
	ds_read_b128 v[62:65], v180 offset:1024
	ds_read_b128 v[66:69], v180 offset:5376
	s_waitcnt lgkmcnt(1)
	v_mfma_f32_16x16x32_bf16 v[86:89], v[62:65], v[58:61], 0
	ds_read_b128 v[62:65], v181 offset:9728
	ds_read_b128 v[90:93], v181 offset:31552
	s_and_b64 vcc, exec, s[74:75]
	s_waitcnt lgkmcnt(2)
	v_mfma_f32_16x16x32_bf16 v[82:85], v[66:69], v[58:61], 0
	ds_read_b128 v[66:69], v181 offset:14080
	s_waitcnt lgkmcnt(2)
	v_mfma_f32_16x16x32_bf16 v[78:81], v[62:65], v[58:61], 0
	ds_read_b128 v[62:65], v180 offset:18496
	s_waitcnt lgkmcnt(1)
	v_mfma_f32_16x16x32_bf16 v[74:77], v[66:69], v[58:61], 0
	ds_read_b128 v[66:69], v180 offset:22848
	s_waitcnt lgkmcnt(1)
	v_mfma_f32_16x16x32_bf16 v[70:73], v[62:65], v[58:61], 0
	ds_read_b128 v[62:65], v181 offset:27200
	s_waitcnt lgkmcnt(1)
	v_mfma_f32_16x16x32_bf16 v[66:69], v[66:69], v[58:61], 0
	s_waitcnt lgkmcnt(0)
	v_mfma_f32_16x16x32_bf16 v[62:65], v[62:65], v[58:61], 0
	v_mfma_f32_16x16x32_bf16 v[58:61], v[90:93], v[58:61], 0
	s_cbranch_vccnz .LBB0_816
	v_readlane_b32 s36, v251, 7
	v_readlane_b32 s37, v251, 8
	v_cndmask_b32_e64 v53, v53, 0, s[94:95]
	v_cndmask_b32_e64 v92, v52, 0, s[34:35]
	v_cndmask_b32_e64 v54, v54, 0, s[36:37]
	v_readlane_b32 s36, v251, 16
	v_readlane_b32 s37, v251, 17
	s_nop 1
	v_cndmask_b32_e64 v55, v55, 0, s[36:37]
	v_readlane_b32 s36, v251, 22
	v_readlane_b32 s37, v251, 23
	s_nop 1
	v_cndmask_b32_e64 v56, v56, 0, s[36:37]
	v_readlane_b32 s36, v251, 24
	v_readlane_b32 s37, v251, 25
	s_nop 1
	v_cndmask_b32_e64 v57, v57, 0, s[36:37]
	v_readlane_b32 s36, v251, 26
	v_readlane_b32 s37, v251, 27
	s_nop 1
	v_cndmask_b32_e64 v90, v50, 0, s[36:37]
	v_readlane_b32 s36, v251, 28
	v_readlane_b32 s37, v251, 29
	v_cvt_pk_bf16_f32 v50, v54, v55
	s_nop 1
	v_cndmask_b32_e64 v91, v51, 0, s[36:37]
	v_cvt_pk_bf16_f32 v51, v56, v57
	v_cvt_pk_bf16_f32 v52, v90, v91
	v_cvt_pk_bf16_f32 v53, v92, v53
	ds_read_b128 v[2:5], v180 offset:1088
	ds_read_b128 v[6:9], v180 offset:5440
	ds_read_b128 v[10:13], v181 offset:9792
	ds_read_b128 v[14:17], v181 offset:14144
	ds_read_b128 v[18:21], v180 offset:18432
	ds_read_b128 v[22:25], v180 offset:22784
	ds_read_b128 v[26:29], v181 offset:27136
	ds_read_b128 v[30:33], v181 offset:31488
	s_waitcnt lgkmcnt(7)
	v_mfma_f32_16x16x32_bf16 v[86:89], v[2:5], v[50:53], v[86:89]
	s_waitcnt lgkmcnt(6)
	v_mfma_f32_16x16x32_bf16 v[82:85], v[6:9], v[50:53], v[82:85]
	s_waitcnt lgkmcnt(5)
	v_mfma_f32_16x16x32_bf16 v[78:81], v[10:13], v[50:53], v[78:81]
	s_waitcnt lgkmcnt(4)
	v_mfma_f32_16x16x32_bf16 v[74:77], v[14:17], v[50:53], v[74:77]
	s_waitcnt lgkmcnt(3)
	v_mfma_f32_16x16x32_bf16 v[70:73], v[18:21], v[50:53], v[70:73]
	s_waitcnt lgkmcnt(2)
	v_mfma_f32_16x16x32_bf16 v[66:69], v[22:25], v[50:53], v[66:69]
	s_waitcnt lgkmcnt(1)
	v_mfma_f32_16x16x32_bf16 v[62:65], v[26:29], v[50:53], v[62:65]
	s_waitcnt lgkmcnt(0)
	v_mfma_f32_16x16x32_bf16 v[58:61], v[30:33], v[50:53], v[58:61]
; #define LAS __attribute__((address_space(3)))
; __device__ __forceinline__ unsigned cvt_pk_bf16(float lo, float hi) { unsigned r; asm volatile("v_cvt_pk_bf16_f32 %0, %1, %2" : "=v"(r) : "v"(lo), "v"(hi)); return r; }
; __device__ __forceinline__ void sg_phase(const Frame& F, const KArgs& a, const int u_first, const int u_count) {
;     ...
;         for (int ks = 0; ks < 4; ++ks) { if (ks > (w >> 1)) continue;
;             const f32x4 w0 = wraw[ks][0], w1 = wraw[ks][1];
;             float wv[8] = {w0[0], w0[1], w0[2], w0[3], w1[0], w1[1], w1[2], w1[3]};
; #pragma unroll
;             for (int i = 0; i < 8; ++i) if (32 * ks + 8 * kq + i > t) wv[i] = 0.f;
;             u32x4 pk; pk.x = cvt_pk_bf16(wv[0], wv[1]); pk.y = cvt_pk_bf16(wv[2], wv[3]); pk.z = cvt_pk_bf16(wv[4], wv[5]); pk.w = cvt_pk_bf16(wv[6], wv[7]);
;             const bf16x8 wf = __builtin_bit_cast(bf16x8, pk);
; #pragma unroll
;             for (int j = 0; j < 8; ++j) { const bf16x8 vf = *(const LAS bf16x8*)(vt + (16 * j + tl) * 136 + ((32 * ks + 8 * kq) ^ ((j >> 1) * 16)));
;                 acc[j] = __builtin_amdgcn_mfma_f32_16x16x32_bf16(vf, wf, acc[j], 0, 0, 0); }
;         }
.LBB0_816:
	s_and_b64 vcc, exec, s[72:73]
	s_cbranch_vccnz .LBB0_818
	v_cndmask_b32_e64 v46, v46, 0, s[96:97]
	v_cndmask_b32_e64 v47, v47, 0, s[20:21]
	v_cndmask_b32_e64 v48, v48, 0, s[22:23]
	v_cndmask_b32_e64 v49, v49, 0, s[24:25]
	v_cndmask_b32_e64 v45, v45, 0, s[52:53]
	v_cndmask_b32_e64 v50, v42, 0, s[26:27]
	v_cndmask_b32_e64 v51, v43, 0, s[28:29]
	v_cndmask_b32_e64 v52, v44, 0, s[30:31]
	v_cvt_pk_bf16_f32 v42, v46, v47
	v_cvt_pk_bf16_f32 v43, v48, v49
	v_cvt_pk_bf16_f32 v44, v50, v51
	v_cvt_pk_bf16_f32 v45, v52, v45
	ds_read_b128 v[2:5], v180 offset:1152
	ds_read_b128 v[6:9], v180 offset:5504
	ds_read_b128 v[10:13], v181 offset:9856
	ds_read_b128 v[14:17], v181 offset:14208
	ds_read_b128 v[18:21], v180 offset:18624
	ds_read_b128 v[22:25], v180 offset:22976
	ds_read_b128 v[26:29], v181 offset:27328
	ds_read_b128 v[30:33], v181 offset:31680
	s_waitcnt lgkmcnt(7)
	v_mfma_f32_16x16x32_bf16 v[86:89], v[2:5], v[42:45], v[86:89]
	s_waitcnt lgkmcnt(6)
	v_mfma_f32_16x16x32_bf16 v[82:85], v[6:9], v[42:45], v[82:85]
	s_waitcnt lgkmcnt(5)
	v_mfma_f32_16x16x32_bf16 v[78:81], v[10:13], v[42:45], v[78:81]
	s_waitcnt lgkmcnt(4)
	v_mfma_f32_16x16x32_bf16 v[74:77], v[14:17], v[42:45], v[74:77]
	s_waitcnt lgkmcnt(3)
	v_mfma_f32_16x16x32_bf16 v[70:73], v[18:21], v[42:45], v[70:73]
	s_waitcnt lgkmcnt(2)
	v_mfma_f32_16x16x32_bf16 v[66:69], v[22:25], v[42:45], v[66:69]
	s_waitcnt lgkmcnt(1)
	v_mfma_f32_16x16x32_bf16 v[62:65], v[26:29], v[42:45], v[62:65]
	s_waitcnt lgkmcnt(0)
	v_mfma_f32_16x16x32_bf16 v[58:61], v[30:33], v[42:45], v[58:61]
.LBB0_818:
	v_readlane_b32 s72, v251, 3
	v_readlane_b32 s73, v251, 4
	s_and_b64 vcc, exec, s[70:71]
	s_cbranch_vccnz .LBB0_803
	v_cndmask_b32_e64 v38, v38, 0, s[54:55]
	v_cndmask_b32_e64 v39, v39, 0, s[56:57]
	v_cndmask_b32_e64 v40, v40, 0, s[58:59]
	v_cndmask_b32_e64 v41, v41, 0, s[60:61]
	v_cndmask_b32_e64 v37, v37, 0, s[68:69]
	v_cndmask_b32_e64 v42, v34, 0, s[62:63]
	v_cndmask_b32_e64 v43, v35, 0, s[64:65]
	v_cndmask_b32_e64 v44, v36, 0, s[66:67]
	v_cvt_pk_bf16_f32 v34, v38, v39
	v_cvt_pk_bf16_f32 v35, v40, v41
	v_cvt_pk_bf16_f32 v36, v42, v43
	v_cvt_pk_bf16_f32 v37, v44, v37
	ds_read_b128 v[2:5], v180 offset:1216
	ds_read_b128 v[6:9], v180 offset:5568
	ds_read_b128 v[10:13], v181 offset:9920
	ds_read_b128 v[14:17], v181 offset:14272
	ds_read_b128 v[18:21], v182 offset:18432
	ds_read_b128 v[22:25], v182 offset:22784
	ds_read_b128 v[26:29], v181 offset:27264
	ds_read_b128 v[30:33], v181 offset:31616
	s_waitcnt lgkmcnt(7)
	v_mfma_f32_16x16x32_bf16 v[86:89], v[2:5], v[34:37], v[86:89]
	s_waitcnt lgkmcnt(6)
	v_mfma_f32_16x16x32_bf16 v[82:85], v[6:9], v[34:37], v[82:85]
	s_waitcnt lgkmcnt(5)
	v_mfma_f32_16x16x32_bf16 v[78:81], v[10:13], v[34:37], v[78:81]
	s_waitcnt lgkmcnt(4)
	v_mfma_f32_16x16x32_bf16 v[74:77], v[14:17], v[34:37], v[74:77]
	s_waitcnt lgkmcnt(3)
	v_mfma_f32_16x16x32_bf16 v[70:73], v[18:21], v[34:37], v[70:73]
	s_waitcnt lgkmcnt(2)
	v_mfma_f32_16x16x32_bf16 v[66:69], v[22:25], v[34:37], v[66:69]
	s_waitcnt lgkmcnt(1)
	v_mfma_f32_16x16x32_bf16 v[62:65], v[26:29], v[34:37], v[62:65]
	s_waitcnt lgkmcnt(0)
	v_mfma_f32_16x16x32_bf16 v[58:61], v[30:33], v[34:37], v[58:61]
	s_branch .LBB0_803
